# grid barrier: non-leader workgroups poll the top generation word directly (no per-XCD relay hop)
# speedup vs baseline: 1.0005x; 1.0005x over previous
.LBB0_236:
	s_or_b64 exec, exec, s[8:9]
	v_cvt_f32_u32_e32 v5, v3
	s_waitcnt vmcnt(0)
	v_readfirstlane_b32 s2, v4
	v_sub_u32_e32 v4, 0, v3
	v_rcp_iflag_f32_e32 v5, v5
	v_add_u32_e32 v6, s2, v2
	v_mul_f32_e32 v5, 0x4f7ffffe, v5
	v_cvt_u32_f32_e32 v5, v5
	v_mul_lo_u32 v2, v4, v5
	v_mul_hi_u32 v2, v5, v2
	v_add_u32_e32 v2, v5, v2
	v_mul_hi_u32 v2, v6, v2
	v_mul_lo_u32 v4, v2, v3
	v_sub_u32_e32 v4, v6, v4
	v_add_u32_e32 v5, 1, v2
	v_cmp_ge_u32_e32 vcc, v4, v3
	s_nop 1
	v_cndmask_b32_e32 v2, v2, v5, vcc
	v_sub_u32_e32 v5, v4, v3
	v_cndmask_b32_e32 v4, v4, v5, vcc
	v_add_u32_e32 v5, 1, v2
	v_cmp_ge_u32_e32 vcc, v4, v3
	v_add_u32_e32 v4, 1, v6
	s_nop 0
	v_cndmask_b32_e32 v2, v2, v5, vcc
	v_mul_lo_u32 v5, v3, v2
	v_add_u32_e32 v3, v5, v3
	v_cmp_ne_u32_e32 vcc, v4, v3
	s_and_saveexec_b64 s[2:3], vcc
	s_xor_b64 s[6:7], exec, s[2:3]
	s_cbranch_execz .LBB0_252
	s_waitcnt lgkmcnt(0)
	v_mov_b32_e32 v1, 0x7500
	global_load_dword v1, v1, s[84:85] sc1
	s_add_u32 s12, s84, 0x7500
	s_addc_u32 s13, s85, 0
	s_waitcnt vmcnt(0)
	v_cmp_eq_u32_e32 vcc, v1, v2
	s_and_saveexec_b64 s[8:9], vcc
	s_cbranch_execz .LBB0_251
	s_add_u32 s10, s84, 0x4200
	s_addc_u32 s11, s85, 0
	s_mov_b32 s2, 1
	s_mov_b64 s[14:15], 0
	v_mov_b32_e32 v1, 0
	s_branch .LBB0_240

.LBB0_784:
	s_or_b64 exec, exec, s[10:11]
	v_cvt_f32_u32_e32 v5, v3
	s_waitcnt vmcnt(0)
	v_readfirstlane_b32 s8, v4
	v_sub_u32_e32 v4, 0, v3
	v_rcp_iflag_f32_e32 v5, v5
	v_add_u32_e32 v6, s8, v2
	v_mul_f32_e32 v5, 0x4f7ffffe, v5
	v_cvt_u32_f32_e32 v5, v5
	v_mul_lo_u32 v2, v4, v5
	v_mul_hi_u32 v2, v5, v2
	v_add_u32_e32 v2, v5, v2
	v_mul_hi_u32 v2, v6, v2
	v_mul_lo_u32 v4, v2, v3
	v_sub_u32_e32 v4, v6, v4
	v_add_u32_e32 v5, 1, v2
	v_cmp_ge_u32_e32 vcc, v4, v3
	s_nop 1
	v_cndmask_b32_e32 v2, v2, v5, vcc
	v_sub_u32_e32 v5, v4, v3
	v_cndmask_b32_e32 v4, v4, v5, vcc
	v_add_u32_e32 v5, 1, v2
	v_cmp_ge_u32_e32 vcc, v4, v3
	v_add_u32_e32 v4, 1, v6
	s_nop 0
	v_cndmask_b32_e32 v2, v2, v5, vcc
	v_mul_lo_u32 v5, v3, v2
	v_add_u32_e32 v3, v5, v3
	v_cmp_ne_u32_e32 vcc, v4, v3
	s_and_saveexec_b64 s[8:9], vcc
	s_xor_b64 s[8:9], exec, s[8:9]
	s_cbranch_execz .LBB0_798
	s_waitcnt lgkmcnt(0)
	v_mov_b32_e32 v1, 0x7500
	global_load_dword v1, v1, s[84:85] sc1
	s_add_u32 s14, s84, 0x7500
	s_addc_u32 s15, s85, 0
	s_waitcnt vmcnt(0)
	v_cmp_eq_u32_e32 vcc, v1, v2
	s_and_saveexec_b64 s[10:11], vcc
	s_cbranch_execz .LBB0_797
	s_add_u32 s12, s84, 0x4200
	s_addc_u32 s13, s85, 0
	s_mov_b32 s26, 1
	s_mov_b64 s[16:17], 0
	v_mov_b32_e32 v1, 0
	s_branch .LBB0_788

.LBB0_952:
	s_or_b64 exec, exec, s[8:9]
	v_cvt_f32_u32_e32 v5, v3
	s_waitcnt vmcnt(0)
	v_readfirstlane_b32 s6, v4
	v_sub_u32_e32 v4, 0, v3
	v_rcp_iflag_f32_e32 v5, v5
	v_add_u32_e32 v6, s6, v2
	v_mul_f32_e32 v5, 0x4f7ffffe, v5
	v_cvt_u32_f32_e32 v5, v5
	v_mul_lo_u32 v2, v4, v5
	v_mul_hi_u32 v2, v5, v2
	v_add_u32_e32 v2, v5, v2
	v_mul_hi_u32 v2, v6, v2
	v_mul_lo_u32 v4, v2, v3
	v_sub_u32_e32 v4, v6, v4
	v_add_u32_e32 v5, 1, v2
	v_cmp_ge_u32_e32 vcc, v4, v3
	s_nop 1
	v_cndmask_b32_e32 v2, v2, v5, vcc
	v_sub_u32_e32 v5, v4, v3
	v_cndmask_b32_e32 v4, v4, v5, vcc
	v_add_u32_e32 v5, 1, v2
	v_cmp_ge_u32_e32 vcc, v4, v3
	v_add_u32_e32 v4, 1, v6
	s_nop 0
	v_cndmask_b32_e32 v2, v2, v5, vcc
	v_mul_lo_u32 v5, v3, v2
	v_add_u32_e32 v3, v5, v3
	v_cmp_ne_u32_e32 vcc, v4, v3
	s_and_saveexec_b64 s[6:7], vcc
	s_xor_b64 s[6:7], exec, s[6:7]
	s_cbranch_execz .LBB0_966
	s_waitcnt lgkmcnt(0)
	v_mov_b32_e32 v1, 0x7500
	global_load_dword v1, v1, s[84:85] sc1
	s_add_u32 s12, s84, 0x7500
	s_addc_u32 s13, s85, 0
	s_waitcnt vmcnt(0)
	v_cmp_eq_u32_e32 vcc, v1, v2
	s_and_saveexec_b64 s[8:9], vcc
	s_cbranch_execz .LBB0_965
	s_add_u32 s10, s84, 0x4200
	s_addc_u32 s11, s85, 0
	s_mov_b32 s24, 1
	s_mov_b64 s[14:15], 0
	v_mov_b32_e32 v1, 0
	s_branch .LBB0_956

.LBB0_1130:
	s_or_b64 exec, exec, s[12:13]
	v_cvt_f32_u32_e32 v5, v3
	s_waitcnt vmcnt(0)
	v_readfirstlane_b32 s10, v4
	v_sub_u32_e32 v4, 0, v3
	v_rcp_iflag_f32_e32 v5, v5
	v_add_u32_e32 v6, s10, v2
	v_mul_f32_e32 v5, 0x4f7ffffe, v5
	v_cvt_u32_f32_e32 v5, v5
	v_mul_lo_u32 v2, v4, v5
	v_mul_hi_u32 v2, v5, v2
	v_add_u32_e32 v2, v5, v2
	v_mul_hi_u32 v2, v6, v2
	v_mul_lo_u32 v4, v2, v3
	v_sub_u32_e32 v4, v6, v4
	v_add_u32_e32 v5, 1, v2
	v_cmp_ge_u32_e32 vcc, v4, v3
	s_nop 1
	v_cndmask_b32_e32 v2, v2, v5, vcc
	v_sub_u32_e32 v5, v4, v3
	v_cndmask_b32_e32 v4, v4, v5, vcc
	v_add_u32_e32 v5, 1, v2
	v_cmp_ge_u32_e32 vcc, v4, v3
	v_add_u32_e32 v4, 1, v6
	s_nop 0
	v_cndmask_b32_e32 v2, v2, v5, vcc
	v_mul_lo_u32 v5, v3, v2
	v_add_u32_e32 v3, v5, v3
	v_cmp_ne_u32_e32 vcc, v4, v3
	s_and_saveexec_b64 s[10:11], vcc
	s_xor_b64 s[10:11], exec, s[10:11]
	s_cbranch_execz .LBB0_1144
	s_waitcnt lgkmcnt(0)
	v_mov_b32_e32 v1, 0x7500
	global_load_dword v1, v1, s[84:85] sc1
	s_add_u32 s16, s84, 0x7500
	s_addc_u32 s17, s85, 0
	s_waitcnt vmcnt(0)
	v_cmp_eq_u32_e32 vcc, v1, v2
	s_and_saveexec_b64 s[12:13], vcc
	s_cbranch_execz .LBB0_1143
	s_add_u32 s14, s84, 0x4200
	s_addc_u32 s15, s85, 0
	s_mov_b32 s28, 1
	s_mov_b64 s[18:19], 0
	v_mov_b32_e32 v1, 0
	s_branch .LBB0_1134

.LBB0_1284:
	s_or_b64 exec, exec, s[8:9]
	v_cvt_f32_u32_e32 v5, v3
	s_waitcnt vmcnt(0)
	v_readfirstlane_b32 s6, v4
	v_sub_u32_e32 v4, 0, v3
	v_rcp_iflag_f32_e32 v5, v5
	v_add_u32_e32 v6, s6, v2
	v_mul_f32_e32 v5, 0x4f7ffffe, v5
	v_cvt_u32_f32_e32 v5, v5
	v_mul_lo_u32 v2, v4, v5
	v_mul_hi_u32 v2, v5, v2
	v_add_u32_e32 v2, v5, v2
	v_mul_hi_u32 v2, v6, v2
	v_mul_lo_u32 v4, v2, v3
	v_sub_u32_e32 v4, v6, v4
	v_add_u32_e32 v5, 1, v2
	v_cmp_ge_u32_e32 vcc, v4, v3
	s_nop 1
	v_cndmask_b32_e32 v2, v2, v5, vcc
	v_sub_u32_e32 v5, v4, v3
	v_cndmask_b32_e32 v4, v4, v5, vcc
	v_add_u32_e32 v5, 1, v2
	v_cmp_ge_u32_e32 vcc, v4, v3
	v_add_u32_e32 v4, 1, v6
	s_nop 0
	v_cndmask_b32_e32 v2, v2, v5, vcc
	v_mul_lo_u32 v5, v3, v2
	v_add_u32_e32 v3, v5, v3
	v_cmp_ne_u32_e32 vcc, v4, v3
	s_and_saveexec_b64 s[6:7], vcc
	s_xor_b64 s[6:7], exec, s[6:7]
	s_cbranch_execz .LBB0_1298
	s_waitcnt lgkmcnt(0)
	v_mov_b32_e32 v1, 0x7500
	global_load_dword v1, v1, s[84:85] sc1
	s_add_u32 s12, s84, 0x7500
	s_addc_u32 s13, s85, 0
	s_waitcnt vmcnt(0)
	v_cmp_eq_u32_e32 vcc, v1, v2
	s_and_saveexec_b64 s[8:9], vcc
	s_cbranch_execz .LBB0_1297
	s_add_u32 s10, s84, 0x4200
	s_addc_u32 s11, s85, 0
	s_mov_b32 s26, 1
	s_mov_b64 s[14:15], 0
	v_mov_b32_e32 v1, 0
	s_branch .LBB0_1288
